# s22 + P4 converters paced (s_sleep 20 per item) so that the memory system is less saturated while the latency-sensitive scan runs
# speedup vs baseline: 1.0002x; 1.0002x over previous
.Lfc4_body0:
	s_sleep 20
	s_add_u32 s2, s2, s33
	s_cmp_lt_u32 s2, s4
	s_cbranch_scc0 .Lfc4_nl0
	s_mov_b32 s26, 39424
	s_add_u32 s29, s2, s26
	s_cmp_lt_u32 s29, 0x10000
	s_cbranch_scc0 .Lfc4_sdb0
	s_lshr_b32 s30, s29, 11
	s_and_b32 s26, s29, 0x7ff
	s_lshr_b32 s31, s26, 7
	s_and_b32 s32, s26, 0x7f
	s_lshl_b32 s26, s30, 25
	s_lshl_b32 s27, s31, 21
	s_add_u32 s26, s26, s27
	s_lshl_b32 s27, s32, 7
	s_add_u32 s26, s26, s27
	s_add_u32 s6, s18, s26
	s_addc_u32 s7, s19, 0
	s_movk_i32 s24, 0x4000
	s_branch .Lfc4_scb0
